# tconv8 channel top: tap and HPART loads issued before the vmcnt(0)+barrier that waits for the previous channel's stores, so their latency overlaps the store drain
# speedup vs baseline: 1.0308x; 1.0008x over previous
.LBB0_438:
	s_add_i32 s38, s36, s30
	s_ashr_i32 s39, s38, 31
	s_lshl_b64 s[4:5], s[38:39], 14
	s_add_u32 s4, s44, s4
	s_addc_u32 s5, s45, s5
	s_addk_i32 s38, 0x600
	s_ashr_i32 s39, s38, 31
	s_lshl_b64 s[38:39], s[38:39], 14
	s_add_u32 s38, s44, s38
	s_addc_u32 s39, s45, s39
	v_mov_b32_e32 v1, v200
	s_movk_i32 s37, 0xff
	s_nop 0
	v_lshlrev_b32_e32 v0, 4, v1
	v_readfirstlane_b32 s98, v1
	s_nop 0
	s_cmp_gt_u32 s98, 0xff
	s_cbranch_scc1 .Lt8_tap_hb
	v_sub_u32_e32 v244, 0xff0, v0
	v_lshl_add_u64 v[2:3], v[244:245], 2, s[4:5]
	s_branch .Lt8_tap_ld

.Lt8_tap_ld:
	global_load_dwordx4 v[20:23], v[2:3], off
	global_load_dwordx4 v[24:27], v[2:3], off offset:16
	global_load_dwordx4 v[28:31], v[2:3], off offset:32
	global_load_dwordx4 v[32:35], v[2:3], off offset:48
	s_ashr_i32 s37, s36, 31
	v_lshl_add_u64 v[18:19], s[36:37], 2, v[176:177]
	global_load_dword v17, v[18:19], off
	s_waitcnt vmcnt(0)
	s_barrier
	s_waitcnt vmcnt(1)
	s_cmp_gt_u32 s98, 0xff
	s_cbranch_scc1 .Lt8_mov_hb
	v_mov_b32_e32 v2, v35
	v_mov_b32_e32 v3, v34
	v_mov_b32_e32 v4, v33
	v_mov_b32_e32 v5, v32
	v_mov_b32_e32 v6, v31
	v_mov_b32_e32 v7, v30
	v_mov_b32_e32 v8, v29
	v_mov_b32_e32 v9, v28
	v_mov_b32_e32 v10, v27
	v_mov_b32_e32 v11, v26
	v_mov_b32_e32 v12, v25
	v_mov_b32_e32 v13, v24
	v_mov_b32_e32 v14, v23
	v_mov_b32_e32 v15, v22
	v_mov_b32_e32 v16, v21
	v_mov_b32_e32 v1, v20
	s_branch .Lt8_mov_done
